# half-workgroup stagger: waves 4-7 s_sleep 4 after barrier B each head so SIMD partner waves are offset
# baseline (speedup 1.0000x reference)
_Z7k_fusedPKDF16_S0_S0_S0_PKfS2_S2_Pf:
	v_lshrrev_b32_e32 v222, 6, v0
	v_and_b32_e32 v1, 63, v0
	s_load_dwordx8 s[24:31], s[0:1], 0x8
	s_load_dwordx4 s[36:39], s[0:1], 0x28
	v_lshlrev_b32_e32 v4, 2, v222
	v_lshlrev_b32_e32 v5, 3, v1
	v_lshl_or_b32 v2, v222, 11, v5
	v_lshlrev_b32_e32 v224, 12, v222
	v_or_b32_e32 v6, 1, v4
	v_lshlrev_b32_e32 v223, 1, v2
	v_readfirstlane_b32 s3, v224
	v_lshl_or_b32 v2, v6, 9, v5
	v_lshlrev_b32_e32 v225, 10, v6
	v_mov_b32_e32 v211, 0
	s_mov_b32 m0, s3
	v_lshlrev_b32_e32 v210, 1, v2
	v_readfirstlane_b32 s3, v225
	s_waitcnt lgkmcnt(0)
	global_load_lds_dwordx4 v223, s[24:25]
	v_lshl_add_u64 v[2:3], s[24:25], 0, v[210:211]
	s_mov_b32 m0, s3
	v_or_b32_e32 v6, 2, v4
	global_load_lds_dwordx4 v[2:3], off
	v_lshl_or_b32 v2, v6, 9, v5
	v_lshlrev_b32_e32 v212, 1, v2
	v_mov_b32_e32 v213, v211
	v_lshl_add_u64 v[2:3], s[24:25], 0, v[212:213]
	v_lshlrev_b32_e32 v213, 10, v6
	v_or_b32_e32 v4, 3, v4
	v_readfirstlane_b32 s3, v213
	s_mov_b32 m0, s3
	v_mov_b32_e32 v215, v211
	global_load_lds_dwordx4 v[2:3], off
	v_lshl_or_b32 v2, v4, 9, v5
	v_lshlrev_b32_e32 v214, 1, v2
	v_lshl_add_u64 v[2:3], s[24:25], 0, v[214:215]
	v_lshlrev_b32_e32 v215, 10, v4
	s_nop 0
	v_readfirstlane_b32 s3, v215
	s_mov_b32 m0, s3
	s_movk_i32 s3, 0xff
	global_load_lds_dwordx4 v[2:3], off
	v_and_b32_e32 v2, 0x7f, v0
	v_lshlrev_b32_e32 v2, 2, v2
	global_load_dword v4, v2, s[36:37]
	global_load_dword v5, v2, s[38:39]
	s_lshl_b32 s3, s2, 8
	s_load_dwordx2 s[4:5], s[0:1], 0x0
	v_and_b32_e32 v6, 0xff, v0
	v_or_b32_e32 v6, s3, v6
	v_ashrrev_i32_e32 v7, 31, v6
	v_lshl_add_u64 v[6:7], v[6:7], 2, s[30:31]
	global_load_dword v244, v[6:7], off
	v_mov_b32_e32 v208, s3
	v_lshl_or_b32 v2, s2, 3, v222
	v_ashrrev_i32_e32 v3, 31, v2
	v_lshlrev_b64 v[2:3], 13, v[2:3]
	s_waitcnt lgkmcnt(0)
	v_lshl_add_u64 v[6:7], s[4:5], 0, v[2:3]
	v_mov_b32_e32 v2, 0
	v_lshlrev_b32_e32 v206, 4, v1
	v_mov_b32_e32 v207, v2
	v_lshl_add_u64 v[6:7], v[6:7], 0, v[206:207]
	v_lshlrev_b32_e32 v211, 13, v222
	v_ashrrev_i32_e32 v209, 31, v208
	v_lshl_add_u64 v[8:9], v[208:209], 2, s[30:31]
	v_or_b32_e32 v3, v211, v206
	v_lshl_add_u64 v[8:9], v[8:9], 0, v[206:207]
	global_load_dwordx4 v[68:71], v[8:9], off
	global_load_dwordx4 v[130:133], v[6:7], off
	global_load_dwordx4 v[134:137], v[6:7], off offset:1024
	global_load_dwordx4 v[138:141], v[6:7], off offset:2048
	global_load_dwordx4 v[142:145], v[6:7], off offset:3072
	s_movk_i32 s33, 0x1000
	v_add_co_u32_e32 v14, vcc, s33, v6
	s_nop 1
	v_addc_co_u32_e32 v15, vcc, 0, v7, vcc
	global_load_dwordx4 v[146:149], v[14:15], off
	global_load_dwordx4 v[150:153], v[14:15], off offset:1024
	global_load_dwordx4 v[154:157], v[14:15], off offset:2048
	global_load_dwordx4 v[158:161], v[14:15], off offset:3072
	v_lshlrev_b32_e32 v10, 1, v3
	global_load_dwordx4 v[186:189], v10, s[28:29] offset:16
	global_load_dwordx4 v[190:193], v10, s[28:29]
	global_load_dwordx4 v[178:181], v10, s[28:29] offset:2064
	global_load_dwordx4 v[182:185], v10, s[28:29] offset:2048
	v_mov_b32_e32 v11, v2
	v_lshl_add_u64 v[8:9], s[28:29], 0, v[10:11]
	v_add_co_u32_e32 v12, vcc, s33, v8
	s_mov_b64 s[34:35], 0x1000
	s_nop 0
	v_addc_co_u32_e32 v13, vcc, 0, v9, vcc
	s_mov_b64 s[40:41], 0x1800
	v_lshl_add_u64 v[10:11], v[8:9], 0, s[34:35]
	v_lshl_add_u64 v[8:9], v[8:9], 0, s[40:41]
	global_load_dwordx4 v[170:173], v[12:13], off
	global_load_dwordx4 v[174:177], v[10:11], off offset:16
	global_load_dwordx4 v[162:165], v[12:13], off offset:2048
	global_load_dwordx4 v[166:169], v[8:9], off offset:16
	s_waitcnt vmcnt(17)
	v_cmp_gt_u32_e32 vcc, 0x100, v0
	s_and_saveexec_b64 s[4:5], vcc
	v_lshlrev_b32_e32 v12, 4, v0
	v_and_b32_e32 v13, 0xe3, v0
	v_lshlrev_b32_e32 v14, 1, v0
	v_and_b32_e32 v12, 64, v12
	s_mov_b32 s8, 0x20000
	v_and_b32_e32 v14, 48, v14
	v_lshl_or_b32 v13, v13, 2, v12
	v_or3_b32 v13, v13, v14, s8
	v_add_f32_e32 v12, -1.0, v244
	v_mul_f32_e32 v12, 0x47000000, v12
	v_mul_f32_e32 v12, 0x3fb8aa3b, v12
	ds_write_b32 v13, v12
	s_or_b64 exec, exec, s[4:5]
	s_waitcnt lgkmcnt(0)
	s_barrier
	ds_read_b128 v[4:7], v206 offset:8192
	ds_read_b128 v[72:75], v206 offset:9216
	s_load_dwordx2 s[30:31], s[0:1], 0x38
	s_mov_b32 s0, 0x47000000
	s_mov_b32 s42, 0x3fb8aa3b
	s_mov_b32 s43, 0xff800000
	v_lshrrev_b32_e32 v96, 5, v1
	v_lshlrev_b32_e32 v97, 4, v96
	v_lshl_or_b32 v209, v222, 11, v206
	v_lshlrev_b32_e32 v1, 5, v1
	s_add_u32 s54, s24, 0x8000
	v_lshlrev_b32_e32 v207, 2, v96
	s_addc_u32 s55, s25, 0
	v_or_b32_e32 v227, 0x10000, v3
	s_mov_b32 s56, 0xc1d00000
	s_mov_b64 s[44:45], 0x20000
	s_mov_b64 s[46:47], 0x20800
	s_mov_b64 s[48:49], 0x21000
	s_mov_b32 s57, 0x21000
	s_mov_b64 s[50:51], 0x21800
	v_mov_b32_e32 v194, 0x3c003c00
	s_waitcnt lgkmcnt(0)
	s_waitcnt vmcnt(15)
	v_mfma_f32_32x32x16_f16 v[36:51], v[4:7], v[130:133], 0
	ds_read_b128 v[4:7], v206
	ds_read_b128 v[76:79], v206 offset:1024
	ds_read_b128 v[20:23], v206 offset:24576
	ds_read_b128 v[80:83], v206 offset:25600
	ds_read_b128 v[52:55], v206 offset:16384
	ds_read_b128 v[84:87], v206 offset:17408
	v_max_f32_e32 v71, v71, v71
	s_waitcnt lgkmcnt(1)
	v_mfma_f32_32x32x16_f16 v[52:67], v[130:133], v[52:55], 0
	v_max_f32_e32 v70, v70, v70
	v_max_f32_e32 v70, v70, v71
	s_waitcnt vmcnt(14)
	v_mfma_f32_32x32x16_f16 v[36:51], v[72:75], v[134:137], v[36:51]
	s_waitcnt lgkmcnt(0)
	v_mfma_f32_32x32x16_f16 v[52:67], v[134:137], v[84:87], v[52:67]
	ds_read_b128 v[72:75], v206 offset:10240
	ds_read_b128 v[84:87], v206 offset:11264
	s_waitcnt lgkmcnt(1)
	s_waitcnt vmcnt(13)
	v_mfma_f32_32x32x16_f16 v[36:51], v[72:75], v[138:141], v[36:51]
	ds_read_b128 v[72:75], v206 offset:18432
	ds_read_b128 v[88:91], v206 offset:19456
	s_waitcnt lgkmcnt(1)
	v_mfma_f32_32x32x16_f16 v[52:67], v[138:141], v[72:75], v[52:67]
	ds_read_b128 v[72:75], v206 offset:12288
	s_waitcnt vmcnt(12)
	v_mfma_f32_32x32x16_f16 v[36:51], v[84:87], v[142:145], v[36:51]
	v_mbcnt_lo_u32_b32 v84, -1, 0
	v_mbcnt_hi_u32_b32 v92, -1, v84
	ds_read_b128 v[84:87], v206 offset:13312
	v_xor_b32_e32 v93, 1, v92
	v_xor_b32_e32 v94, 2, v92
	v_xor_b32_e32 v95, 4, v92
	s_waitcnt lgkmcnt(2)
	v_mfma_f32_32x32x16_f16 v[52:67], v[142:145], v[88:91], v[52:67]
	v_and_b32_e32 v88, 64, v92
	v_add_u32_e32 v98, 64, v88
	v_cmp_lt_i32_e32 vcc, v93, v98
	ds_read_b128 v[88:91], v206 offset:21504
	s_waitcnt lgkmcnt(2)
	s_waitcnt vmcnt(11)
	v_mfma_f32_32x32x16_f16 v[36:51], v[72:75], v[146:149], v[36:51]
	ds_read_b128 v[72:75], v206 offset:20480
	s_waitcnt lgkmcnt(0)
	v_mfma_f32_32x32x16_f16 v[52:67], v[146:149], v[72:75], v[52:67]
	v_cndmask_b32_e32 v72, v92, v93, vcc
	v_lshlrev_b32_e32 v72, 2, v72
	v_max3_f32 v73, v68, v69, v70
	ds_bpermute_b32 v72, v72, v73
	v_cmp_lt_i32_e32 vcc, v94, v98
	s_waitcnt lgkmcnt(0)
	v_max_f32_e32 v72, v72, v72
	v_cndmask_b32_e32 v68, v92, v94, vcc
	v_lshlrev_b32_e32 v74, 2, v68
	ds_read_b128 v[68:71], v206 offset:14336
	s_waitcnt vmcnt(10)
	v_mfma_f32_32x32x16_f16 v[36:51], v[84:87], v[150:153], v[36:51]
	v_max_f32_e32 v84, v73, v72
	ds_bpermute_b32 v85, v74, v84
	v_cmp_lt_i32_e32 vcc, v95, v98
	s_waitcnt lgkmcnt(0)
	v_max_f32_e32 v85, v85, v85
	v_mfma_f32_32x32x16_f16 v[52:67], v[150:153], v[88:91], v[52:67]
	v_cndmask_b32_e32 v72, v92, v95, vcc
	v_lshlrev_b32_e32 v86, 2, v72
	v_max_f32_e32 v92, v84, v85
	ds_read_b128 v[72:75], v206 offset:15360
	ds_bpermute_b32 v93, v86, v92
	s_waitcnt lgkmcnt(0)
	v_max_f32_e32 v93, v93, v93
	s_waitcnt vmcnt(9)
	v_mfma_f32_32x32x16_f16 v[36:51], v[68:71], v[154:157], v[36:51]
	ds_read_b128 v[68:71], v206 offset:22528
	ds_read_b128 v[84:87], v206 offset:23552
	v_max_f32_e32 v92, v92, v93
	global_load_dwordx4 v[88:91], v97, s[36:37]
	v_readlane_b32 s3, v92, 0
	v_readlane_b32 s2, v92, 8
	v_readlane_b32 s5, v92, 16
	v_readlane_b32 s4, v92, 24
	s_waitcnt lgkmcnt(1)
	v_mfma_f32_32x32x16_f16 v[52:67], v[154:157], v[68:71], v[52:67]
	v_add_f32_e64 v68, s2, -1.0
	v_add_f32_e64 v69, s3, -1.0
	v_readlane_b32 s7, v92, 32
	v_readlane_b32 s6, v92, 40
	v_add_f32_e64 v70, s4, -1.0
	v_add_f32_e64 v71, s5, -1.0
	v_pk_mul_f32 v[68:69], v[68:69], s[0:1] op_sel_hi:[1,0]
	v_readlane_b32 s9, v92, 48
	v_readlane_b32 s8, v92, 56
	v_mfma_f32_32x32x16_f16 v[20:35], v[20:23], v[130:133], 0
	v_mul_f32_e64 v70, v70, s0
	v_mul_f32_e64 v71, v71, s0
	v_mul_f32_e64 v92, v68, s42
	v_mul_f32_e64 v93, v69, s42
	v_mul_f32_e64 v94, v70, s42
	v_mul_f32_e64 v95, v71, s42
	v_max3_f32 v68, v93, s43, v92
	v_max3_f32 v68, v68, v95, v94
	s_waitcnt vmcnt(9)
	v_mfma_f32_32x32x16_f16 v[36:51], v[72:75], v[158:161], v[36:51]
	v_add_f32_e64 v72, s6, -1.0
	v_add_f32_e64 v73, s7, -1.0
	v_mul_f32_e64 v72, v72, s0
	v_mul_f32_e64 v73, v73, s0
	s_waitcnt lgkmcnt(0)
	v_mfma_f32_32x32x16_f16 v[52:67], v[158:161], v[84:87], v[52:67]
	v_mul_f32_e64 v84, v72, s42
	v_mul_f32_e64 v85, v73, s42
	v_add_f32_e64 v86, s8, -1.0
	v_add_f32_e64 v87, s9, -1.0
	v_max3_f32 v98, v68, v85, v84
	ds_read_b128 v[68:71], v206 offset:26624
	v_cvt_pk_f16_f32 v43, v42, v43
	v_cvt_pk_f16_f32 v42, v40, v41
	v_cvt_pk_f16_f32 v41, v38, v39
	v_mfma_f32_32x32x16_f16 v[20:35], v[80:83], v[134:137], v[20:35]
	v_mul_f32_e64 v80, v86, s0
	v_mul_f32_e64 v81, v87, s0
	v_cvt_pk_f16_f32 v40, v36, v37
	v_mul_f32_e64 v86, v80, s42
	v_mul_f32_e64 v87, v81, s42
	global_load_dwordx4 v[72:75], v97, s[36:37] offset:32
	v_max3_f32 v80, v98, v87, v86
	v_add_f32_e32 v98, 0xc53b8000, v80
	ds_read_b128 v[80:83], v206 offset:27648
	global_load_dwordx4 v[36:39], v97, s[36:37] offset:64
	ds_write_b128 v209, v[40:43] offset:32768
	v_cvt_pk_f16_f32 v43, v50, v51
	v_cvt_pk_f16_f32 v40, v44, v45
	v_cvt_pk_f16_f32 v44, v52, v53
	global_load_dwordx4 v[50:53], v97, s[36:37] offset:96
	s_waitcnt lgkmcnt(2)
	v_mfma_f32_32x32x16_f16 v[20:35], v[68:71], v[138:141], v[20:35]
	ds_read_b128 v[68:71], v206 offset:28672
	v_cvt_pk_f16_f32 v42, v48, v49
	v_cvt_pk_f16_f32 v41, v46, v47
	ds_write_b128 v209, v[40:43] offset:33792
	ds_read_b128 v[40:43], v206 offset:30720
	v_cvt_pk_f16_f32 v47, v58, v59
	v_cvt_pk_f16_f32 v46, v56, v57
	s_waitcnt lgkmcnt(4)
	v_mfma_f32_32x32x16_f16 v[20:35], v[80:83], v[142:145], v[20:35]
	ds_read_b128 v[80:83], v206 offset:29696
	v_cvt_pk_f16_f32 v45, v54, v55
	ds_write_b128 v209, v[44:47] offset:49152
	v_cvt_pk_f16_f32 v45, v66, v67
	ds_read_b128 v[46:49], v206 offset:31744
	v_cvt_pk_f16_f32 v44, v64, v65
	v_cmp_ge_f32_e64 s[0:1], v92, v98
	s_waitcnt lgkmcnt(5)
	v_mfma_f32_32x32x16_f16 v[20:35], v[68:71], v[146:149], v[20:35]
	v_cmp_ge_f32_e64 s[2:3], v93, v98
	v_cmp_ge_f32_e64 s[4:5], v94, v98
	v_cmp_ge_f32_e64 s[6:7], v95, v98
	v_cmp_ge_f32_e64 s[8:9], v84, v98
	v_cmp_ge_f32_e64 s[10:11], v85, v98
	v_cmp_ge_f32_e64 s[12:13], v86, v98
	v_cmp_ge_f32_e64 s[14:15], v87, v98
	v_mfma_f32_32x32x16_f16 v[4:19], v[4:7], v[130:133], 0
	s_waitcnt lgkmcnt(2)
	v_mfma_f32_32x32x16_f16 v[20:35], v[80:83], v[150:153], v[20:35]
	v_mfma_f32_32x32x16_f16 v[4:19], v[76:79], v[134:137], v[4:19]
	v_mfma_f32_32x32x16_f16 v[20:35], v[40:43], v[154:157], v[20:35]
	v_cvt_pk_f16_f32 v43, v62, v63
	v_cvt_pk_f16_f32 v42, v60, v61
	ds_write_b128 v209, v[42:45] offset:50176
	ds_read_b128 v[40:43], v206 offset:2048
	ds_read_b128 v[54:57], v206 offset:3072
	s_waitcnt lgkmcnt(1)
	v_mfma_f32_32x32x16_f16 v[4:19], v[40:43], v[138:141], v[4:19]
	s_waitcnt lgkmcnt(0)
	v_mfma_f32_32x32x16_f16 v[4:19], v[54:57], v[142:145], v[4:19]
	v_mfma_f32_32x32x16_f16 v[20:35], v[46:49], v[158:161], v[20:35]
	ds_read_b128 v[44:47], v206 offset:4096
	ds_read_b128 v[58:61], v206 offset:5120
	ds_read_b128 v[62:65], v206 offset:6144
	ds_read_b128 v[66:69], v206 offset:7168
	s_waitcnt lgkmcnt(0)
	s_barrier
	s_waitcnt vmcnt(3)
	s_nop 4
	v_add_f32_e32 v20, v20, v88
	v_mfma_f32_32x32x16_f16 v[4:19], v[44:47], v[146:149], v[4:19]
	v_add_f32_e32 v21, v89, v21
	v_add_f32_e32 v22, v90, v22
	v_add_f32_e32 v23, v91, v23
	s_waitcnt vmcnt(2)
	v_add_f32_e32 v24, v24, v72
	v_add_f32_e32 v25, v73, v25
	v_add_f32_e32 v26, v74, v26
	v_add_f32_e32 v27, v75, v27
	v_mfma_f32_32x32x16_f16 v[4:19], v[58:61], v[150:153], v[4:19]
	s_waitcnt vmcnt(1)
	v_add_f32_e32 v28, v28, v36
	v_add_f32_e32 v29, v37, v29
	v_add_f32_e32 v30, v38, v30
	v_add_f32_e32 v31, v39, v31
	s_waitcnt vmcnt(0)
	v_add_f32_e32 v32, v32, v50
	v_add_f32_e32 v33, v51, v33
	v_add_f32_e32 v34, v52, v34
	v_mfma_f32_32x32x16_f16 v[4:19], v[62:65], v[154:157], v[4:19]
	v_add_f32_e32 v35, v53, v35
	v_mul_f32_e32 v20, 0xbfb8aa3b, v20
	v_mul_f32_e32 v21, 0xbfb8aa3b, v21
	v_mul_f32_e32 v22, 0xbfb8aa3b, v22
	v_mul_f32_e32 v23, 0xbfb8aa3b, v23
	v_mul_f32_e32 v24, 0xbfb8aa3b, v24
	v_mul_f32_e32 v25, 0xbfb8aa3b, v25
	v_mfma_f32_32x32x16_f16 v[4:19], v[66:69], v[158:161], v[4:19]
	v_mul_f32_e32 v26, 0xbfb8aa3b, v26
	v_mul_f32_e32 v27, 0xbfb8aa3b, v27
	v_mul_f32_e32 v28, 0xbfb8aa3b, v28
	v_mul_f32_e32 v29, 0xbfb8aa3b, v29
	v_mul_f32_e32 v30, 0xbfb8aa3b, v30
	v_mul_f32_e32 v31, 0xbfb8aa3b, v31
	v_mul_f32_e32 v32, 0xbfb8aa3b, v32
	v_mul_f32_e32 v33, 0xbfb8aa3b, v33
	v_mul_f32_e32 v34, 0xbfb8aa3b, v34
	v_mul_f32_e32 v35, 0xbfb8aa3b, v35
	v_exp_f32_e32 v20, v20
	v_exp_f32_e32 v21, v21
	v_exp_f32_e32 v22, v22
	v_exp_f32_e32 v23, v23
	v_exp_f32_e32 v24, v24
	v_exp_f32_e32 v25, v25
	v_exp_f32_e32 v26, v26
	v_exp_f32_e32 v27, v27
	v_exp_f32_e32 v28, v28
	v_exp_f32_e32 v29, v29
	v_exp_f32_e32 v30, v30
	v_exp_f32_e32 v31, v31
	v_exp_f32_e32 v32, v32
	v_exp_f32_e32 v33, v33
	v_exp_f32_e32 v34, v34
	v_exp_f32_e32 v35, v35
	v_add_f32_e32 v20, 1.0, v20
	v_add_f32_e32 v21, 1.0, v21
	v_add_f32_e32 v22, 1.0, v22
	v_add_f32_e32 v23, 1.0, v23
	v_add_f32_e32 v24, 1.0, v24
	v_add_f32_e32 v25, 1.0, v25
	v_add_f32_e32 v26, 1.0, v26
	v_add_f32_e32 v27, 1.0, v27
	v_add_f32_e32 v28, 1.0, v28
	v_add_f32_e32 v29, 1.0, v29
	v_add_f32_e32 v30, 1.0, v30
	v_add_f32_e32 v31, 1.0, v31
	v_add_f32_e32 v32, 1.0, v32
	v_add_f32_e32 v33, 1.0, v33
	v_add_f32_e32 v34, 1.0, v34
	v_add_f32_e32 v35, 1.0, v35
	v_rcp_f32_e32 v20, v20
	v_rcp_f32_e32 v21, v21
	v_rcp_f32_e32 v22, v22
	v_rcp_f32_e32 v23, v23
	v_rcp_f32_e32 v24, v24
	v_rcp_f32_e32 v25, v25
	v_rcp_f32_e32 v26, v26
	v_rcp_f32_e32 v27, v27
	v_rcp_f32_e32 v28, v28
	v_rcp_f32_e32 v29, v29
	v_rcp_f32_e32 v30, v30
	v_rcp_f32_e32 v31, v31
	v_rcp_f32_e32 v32, v32
	v_rcp_f32_e32 v33, v33
	v_rcp_f32_e32 v34, v34
	v_rcp_f32_e32 v35, v35
	v_cvt_pk_f16_f32 v198, v4, v5
	v_lshl_or_b32 v4, v222, 14, v1
	v_mov_b32_e32 v5, v2
	v_lshl_add_u64 v[216:217], s[28:29], 0, v[4:5]
	v_or_b32_e32 v4, 0x2000, v4
	v_lshrrev_b32_e32 v1, 1, v0
	v_lshl_add_u64 v[218:219], s[28:29], 0, v[4:5]
	v_and_b32_e32 v4, 16, v1
	v_mov_b32_e32 v36, 0x20000
	v_lshl_add_u64 v[4:5], s[36:37], 0, v[4:5]
	s_mov_b64 s[28:29], 0x80
	v_lshl_or_b32 v226, v96, 6, v36
	v_cvt_pk_f16_f32 v199, v6, v7
	v_cvt_pk_f16_f32 v200, v8, v9
	v_cvt_pk_f16_f32 v201, v10, v11
	v_cvt_pk_f16_f32 v202, v12, v13
	v_cvt_pk_f16_f32 v203, v14, v15
	v_cvt_pk_f16_f32 v204, v16, v17
	v_cvt_pk_f16_f32 v205, v18, v19
	v_cvt_pk_f16_f32 v229, v20, v21
	v_cvt_pk_f16_f32 v230, v22, v23
	v_cvt_pk_f16_f32 v232, v24, v25
	v_cvt_pk_f16_f32 v234, v26, v27
	v_cvt_pk_f16_f32 v228, v28, v29
	v_cvt_pk_f16_f32 v231, v30, v31
	v_cvt_pk_f16_f32 v233, v32, v33
	v_cvt_pk_f16_f32 v235, v34, v35
	v_lshl_add_u64 v[220:221], v[4:5], 0, s[28:29]
	s_mov_b64 s[36:37], 0
	v_readfirstlane_b32 s63, v222
	s_nop 3
	s_branch .LBB1_6

.LBB1_59:
	s_setprio 0
	s_nop 10
	v_rcp_f32_e32 v8, v82
	v_cvt_f32_f16_sdwa v5, v229 dst_sel:DWORD dst_unused:UNUSED_PAD src0_sel:WORD_1
	v_cvt_f32_f16_e32 v4, v229
	v_cvt_f32_f16_sdwa v7, v230 dst_sel:DWORD dst_unused:UNUSED_PAD src0_sel:WORD_1
	v_cvt_f32_f16_e32 v6, v230
	v_cvt_f32_f16_sdwa v11, v232 dst_sel:DWORD dst_unused:UNUSED_PAD src0_sel:WORD_1
	v_cvt_f32_f16_e32 v10, v232
	v_cvt_f32_f16_sdwa v13, v234 dst_sel:DWORD dst_unused:UNUSED_PAD src0_sel:WORD_1
	v_cvt_f32_f16_e32 v12, v234
	v_pk_mul_f32 v[4:5], v[8:9], v[4:5] op_sel_hi:[0,1]
	v_pk_mul_f32 v[6:7], v[8:9], v[6:7] op_sel_hi:[0,1]
	v_pk_mul_f32 v[4:5], v[98:99], v[4:5]
	v_pk_mul_f32 v[6:7], v[100:101], v[6:7]
	v_cvt_pk_f16_f32 v4, v4, v5
	v_cvt_pk_f16_f32 v5, v6, v7
	v_pk_mul_f32 v[6:7], v[8:9], v[10:11] op_sel_hi:[0,1]
	v_pk_mul_f32 v[10:11], v[8:9], v[12:13] op_sel_hi:[0,1]
	v_pk_mul_f32 v[6:7], v[102:103], v[6:7]
	v_pk_mul_f32 v[10:11], v[104:105], v[10:11]
	v_cvt_pk_f16_f32 v6, v6, v7
	v_cvt_pk_f16_f32 v7, v10, v11
	v_cvt_f32_f16_sdwa v11, v228 dst_sel:DWORD dst_unused:UNUSED_PAD src0_sel:WORD_1
	v_cvt_f32_f16_e32 v10, v228
	ds_write_b128 v227, v[4:7]
	v_cvt_f32_f16_sdwa v7, v231 dst_sel:DWORD dst_unused:UNUSED_PAD src0_sel:WORD_1
	v_cvt_f32_f16_e32 v6, v231
	v_pk_mul_f32 v[4:5], v[8:9], v[10:11] op_sel_hi:[0,1]
	v_cvt_f32_f16_sdwa v11, v233 dst_sel:DWORD dst_unused:UNUSED_PAD src0_sel:WORD_1
	v_cvt_f32_f16_e32 v10, v233
	v_cvt_f32_f16_sdwa v13, v235 dst_sel:DWORD dst_unused:UNUSED_PAD src0_sel:WORD_1
	v_cvt_f32_f16_e32 v12, v235
	v_pk_mul_f32 v[6:7], v[8:9], v[6:7] op_sel_hi:[0,1]
	v_pk_mul_f32 v[4:5], v[4:5], v[106:107]
	v_pk_mul_f32 v[6:7], v[6:7], v[108:109]
	v_cvt_pk_f16_f32 v4, v4, v5
	v_cvt_pk_f16_f32 v5, v6, v7
	v_pk_mul_f32 v[6:7], v[8:9], v[10:11] op_sel_hi:[0,1]
	v_pk_mul_f32 v[8:9], v[8:9], v[12:13] op_sel_hi:[0,1]
	v_pk_mul_f32 v[6:7], v[6:7], v[110:111]
	v_pk_mul_f32 v[8:9], v[8:9], v[112:113]
	v_cvt_pk_f16_f32 v6, v6, v7
	v_cvt_pk_f16_f32 v7, v8, v9
	s_and_b64 vcc, exec, s[16:17]
	ds_write_b128 v227, v[4:7] offset:1024
	s_waitcnt vmcnt(0) lgkmcnt(2)
	s_barrier
	s_cbranch_vccnz .LBB1_5
	ds_read_b128 v[4:7], v206 offset:8192
	ds_read_b128 v[8:11], v206 offset:9216
	s_waitcnt lgkmcnt(1)
	v_mfma_f32_32x32x16_f16 v[114:129], v[4:7], v[130:133], 0
	ds_read_b128 v[4:7], v206 offset:16384
	ds_read_b128 v[12:15], v206 offset:17408
	s_waitcnt lgkmcnt(1)
	v_mfma_f32_32x32x16_f16 v[98:113], v[130:133], v[4:7], 0
	v_mfma_f32_32x32x16_f16 v[114:129], v[8:11], v[134:137], v[114:129]
	ds_read_b128 v[4:7], v206 offset:10240
	ds_read_b128 v[8:11], v206 offset:11264
	s_waitcnt lgkmcnt(2)
	v_mfma_f32_32x32x16_f16 v[98:113], v[134:137], v[12:15], v[98:113]
	s_waitcnt lgkmcnt(1)
	v_mfma_f32_32x32x16_f16 v[114:129], v[4:7], v[138:141], v[114:129]
	ds_read_b128 v[4:7], v206 offset:18432
	ds_read_b128 v[12:15], v206 offset:19456
	s_waitcnt lgkmcnt(1)
	v_mfma_f32_32x32x16_f16 v[98:113], v[138:141], v[4:7], v[98:113]
	v_mfma_f32_32x32x16_f16 v[114:129], v[8:11], v[142:145], v[114:129]
	ds_read_b128 v[4:7], v206 offset:12288
	ds_read_b128 v[8:11], v206 offset:13312
	s_waitcnt lgkmcnt(2)
	v_mfma_f32_32x32x16_f16 v[98:113], v[142:145], v[12:15], v[98:113]
	s_waitcnt lgkmcnt(1)
	v_mfma_f32_32x32x16_f16 v[114:129], v[4:7], v[146:149], v[114:129]
	ds_read_b128 v[4:7], v206 offset:20480
	ds_read_b128 v[12:15], v206 offset:21504
	s_waitcnt lgkmcnt(1)
	v_mfma_f32_32x32x16_f16 v[98:113], v[146:149], v[4:7], v[98:113]
	v_mfma_f32_32x32x16_f16 v[114:129], v[8:11], v[150:153], v[114:129]
	ds_read_b128 v[4:7], v206 offset:14336
	ds_read_b128 v[8:11], v206 offset:15360
	s_waitcnt lgkmcnt(2)
	v_mfma_f32_32x32x16_f16 v[98:113], v[150:153], v[12:15], v[98:113]
	s_waitcnt lgkmcnt(1)
	v_mfma_f32_32x32x16_f16 v[114:129], v[4:7], v[154:157], v[114:129]
	ds_read_b128 v[4:7], v206 offset:22528
	ds_read_b128 v[12:15], v206 offset:23552
	s_waitcnt lgkmcnt(1)
	v_mfma_f32_32x32x16_f16 v[98:113], v[154:157], v[4:7], v[98:113]
	v_mfma_f32_32x32x16_f16 v[114:129], v[8:11], v[158:161], v[114:129]
	ds_read_b128 v[4:7], v206 offset:24576
	ds_read_b128 v[8:11], v206 offset:25600
	s_waitcnt lgkmcnt(1)
	v_mfma_f32_32x32x16_f16 v[82:97], v[4:7], v[130:133], 0
	global_load_dwordx4 v[4:7], v[220:221], off
	s_nop 6
	v_cvt_pk_f16_f32 v121, v120, v121
	v_cvt_pk_f16_f32 v120, v118, v119
	v_cvt_pk_f16_f32 v119, v116, v117
	v_cvt_pk_f16_f32 v118, v114, v115
	v_cvt_pk_f16_f32 v117, v128, v129
	v_cvt_pk_f16_f32 v116, v126, v127
	s_waitcnt lgkmcnt(0)
	v_mfma_f32_32x32x16_f16 v[82:97], v[8:11], v[134:137], v[82:97]
	v_cvt_pk_f16_f32 v115, v124, v125
	v_cvt_pk_f16_f32 v114, v122, v123
	v_mfma_f32_32x32x16_f16 v[98:113], v[158:161], v[12:15], v[98:113]
	ds_read_b128 v[8:11], v206 offset:26624
	ds_read_b128 v[12:15], v206 offset:27648
	ds_read_b128 v[196:199], v206 offset:28672
	ds_write_b128 v209, v[114:117] offset:33792
	global_load_dwordx4 v[114:117], v[220:221], off offset:96
	ds_write_b128 v209, v[118:121] offset:32768
	ds_read_b128 v[118:121], v206 offset:29696
	s_nop 4
	v_cvt_pk_f16_f32 v105, v104, v105
	s_waitcnt lgkmcnt(5)
	v_mfma_f32_32x32x16_f16 v[82:97], v[8:11], v[138:141], v[82:97]
	global_load_dwordx4 v[8:11], v[220:221], off offset:32
	v_cvt_pk_f16_f32 v104, v102, v103
	v_cvt_pk_f16_f32 v103, v100, v101
	v_cvt_pk_f16_f32 v102, v98, v99
	ds_read_b128 v[98:101], v206 offset:30720
	ds_write_b128 v209, v[102:105] offset:49152
	v_cvt_pk_f16_f32 v103, v108, v109
	s_waitcnt lgkmcnt(6)
	v_mfma_f32_32x32x16_f16 v[82:97], v[12:15], v[142:145], v[82:97]
	global_load_dwordx4 v[12:15], v[220:221], off offset:64
	v_cvt_pk_f16_f32 v102, v106, v107
	ds_read_b128 v[106:109], v206 offset:31744
	v_cvt_pk_f16_f32 v105, v112, v113
	v_cvt_pk_f16_f32 v104, v110, v111
	ds_write_b128 v209, v[102:105] offset:50176
	s_waitcnt lgkmcnt(7)
	v_mfma_f32_32x32x16_f16 v[82:97], v[196:199], v[146:149], v[82:97]
	s_waitcnt lgkmcnt(4)
	v_mfma_f32_32x32x16_f16 v[82:97], v[118:121], v[150:153], v[82:97]
	s_waitcnt lgkmcnt(3)
	v_mfma_f32_32x32x16_f16 v[82:97], v[98:101], v[154:157], v[82:97]
	ds_read_b128 v[98:101], v206
	ds_read_b128 v[118:121], v206 offset:1024
	ds_read_b128 v[122:125], v206 offset:2048
	ds_read_b128 v[126:129], v206 offset:3072
	ds_read_b128 v[196:199], v206 offset:4096
	ds_read_b128 v[200:203], v206 offset:5120
	ds_read_b128 v[230:233], v206 offset:6144
	ds_read_b128 v[236:239], v206 offset:7168
	s_waitcnt lgkmcnt(0)
	s_barrier
	s_cmp_ge_u32 s63, 4
	s_cbranch_scc0 .Lstag_skip
	s_sleep 4
.Lstag_skip:
	v_mfma_f32_32x32x16_f16 v[82:97], v[106:109], v[158:161], v[82:97]
	v_mfma_f32_32x32x16_f16 v[98:113], v[98:101], v[130:133], 0
	s_waitcnt vmcnt(3)
	s_nop 9
	v_add_f32_e32 v1, v82, v4
	v_mfma_f32_32x32x16_f16 v[98:113], v[118:121], v[134:137], v[98:113]
	v_add_f32_e32 v3, v5, v83
	v_add_f32_e32 v4, v6, v84
	v_add_f32_e32 v5, v7, v85
	v_mul_f32_e32 v1, 0xbfb8aa3b, v1
	v_mul_f32_e32 v3, 0xbfb8aa3b, v3
	v_mul_f32_e32 v4, 0xbfb8aa3b, v4
	v_mul_f32_e32 v5, 0xbfb8aa3b, v5
	v_mfma_f32_32x32x16_f16 v[98:113], v[122:125], v[138:141], v[98:113]
	v_exp_f32_e32 v1, v1
	v_exp_f32_e32 v3, v3
	v_exp_f32_e32 v4, v4
	v_exp_f32_e32 v5, v5
	v_add_f32_e32 v1, 1.0, v1
	v_add_f32_e32 v3, 1.0, v3
	v_add_f32_e32 v4, 1.0, v4
	v_mfma_f32_32x32x16_f16 v[98:113], v[126:129], v[142:145], v[98:113]
	v_add_f32_e32 v5, 1.0, v5
	s_waitcnt vmcnt(2)
	v_add_f32_e32 v16, v116, v96
	v_add_f32_e32 v17, v117, v97
	v_mul_f32_e32 v16, 0xbfb8aa3b, v16
	v_mul_f32_e32 v17, 0xbfb8aa3b, v17
	v_exp_f32_e32 v16, v16
	v_exp_f32_e32 v17, v17
	v_mfma_f32_32x32x16_f16 v[98:113], v[196:199], v[146:149], v[98:113]
	s_waitcnt vmcnt(1)
	v_add_f32_e32 v6, v86, v8
	v_add_f32_e32 v7, v9, v87
	v_add_f32_e32 v8, v10, v88
	v_add_f32_e32 v9, v11, v89
	v_mul_f32_e32 v6, 0xbfb8aa3b, v6
	v_mul_f32_e32 v7, 0xbfb8aa3b, v7
	v_mul_f32_e32 v8, 0xbfb8aa3b, v8
	v_mfma_f32_32x32x16_f16 v[98:113], v[200:203], v[150:153], v[98:113]
	s_waitcnt vmcnt(0)
	v_add_f32_e32 v10, v90, v12
	v_add_f32_e32 v11, v13, v91
	v_add_f32_e32 v12, v14, v92
	v_add_f32_e32 v13, v15, v93
	v_add_f32_e32 v14, v94, v114
	v_add_f32_e32 v15, v115, v95
	v_mul_f32_e32 v9, 0xbfb8aa3b, v9
	v_mfma_f32_32x32x16_f16 v[98:113], v[230:233], v[154:157], v[98:113]
	v_mul_f32_e32 v10, 0xbfb8aa3b, v10
	v_mul_f32_e32 v11, 0xbfb8aa3b, v11
	v_mul_f32_e32 v12, 0xbfb8aa3b, v12
	v_mul_f32_e32 v13, 0xbfb8aa3b, v13
	v_mul_f32_e32 v14, 0xbfb8aa3b, v14
	v_mul_f32_e32 v15, 0xbfb8aa3b, v15
	v_exp_f32_e32 v6, v6
	v_exp_f32_e32 v7, v7
	v_exp_f32_e32 v8, v8
	v_exp_f32_e32 v9, v9
	v_exp_f32_e32 v10, v10
	v_exp_f32_e32 v11, v11
	v_exp_f32_e32 v12, v12
	v_exp_f32_e32 v13, v13
	v_exp_f32_e32 v14, v14
	v_exp_f32_e32 v15, v15
	v_mfma_f32_32x32x16_f16 v[98:113], v[236:239], v[158:161], v[98:113]
	v_add_f32_e32 v6, 1.0, v6
	v_add_f32_e32 v7, 1.0, v7
	v_add_f32_e32 v8, 1.0, v8
	v_add_f32_e32 v9, 1.0, v9
	v_add_f32_e32 v10, 1.0, v10
	v_add_f32_e32 v11, 1.0, v11
	v_add_f32_e32 v12, 1.0, v12
	v_add_f32_e32 v13, 1.0, v13
	v_add_f32_e32 v14, 1.0, v14
	v_add_f32_e32 v15, 1.0, v15
	v_add_f32_e32 v16, 1.0, v16
	v_add_f32_e32 v17, 1.0, v17
	v_rcp_f32_e32 v1, v1
	v_rcp_f32_e32 v3, v3
	v_rcp_f32_e32 v4, v4
	v_rcp_f32_e32 v5, v5
	v_rcp_f32_e32 v6, v6
	v_rcp_f32_e32 v7, v7
	v_rcp_f32_e32 v8, v8
	v_rcp_f32_e32 v9, v9
	v_rcp_f32_e32 v10, v10
	v_rcp_f32_e32 v11, v11
	v_rcp_f32_e32 v12, v12
	v_rcp_f32_e32 v13, v13
	v_rcp_f32_e32 v14, v14
	v_rcp_f32_e32 v15, v15
	v_rcp_f32_e32 v16, v16
	v_rcp_f32_e32 v17, v17
	v_cvt_pk_f16_f32 v228, v10, v11
	v_cvt_pk_f16_f32 v231, v12, v13
	v_cvt_pk_f16_f32 v233, v14, v15
	v_cvt_pk_f16_f32 v235, v16, v17
	v_cvt_pk_f16_f32 v229, v1, v3
	v_cvt_pk_f16_f32 v230, v4, v5
	v_cvt_pk_f16_f32 v232, v6, v7
	v_cvt_pk_f16_f32 v234, v8, v9
	v_cvt_pk_f16_f32 v202, v106, v107
	v_cvt_pk_f16_f32 v203, v108, v109
	v_cvt_pk_f16_f32 v204, v110, v111
	v_cvt_pk_f16_f32 v205, v112, v113
	v_cvt_pk_f16_f32 v198, v98, v99
	v_cvt_pk_f16_f32 v199, v100, v101
	v_cvt_pk_f16_f32 v200, v102, v103
	v_cvt_pk_f16_f32 v201, v104, v105
	s_branch .LBB1_5
